# gdn_scan: next chunk's u0 loads spread into the gaps of the qk*v_new MFMA batch instead of one burst, on top of v90
# speedup vs baseline: 1.0090x; 1.0090x over previous
.LBB0_490:
	s_bitcmp1_b32 s35, 0
	s_cselect_b32 s26, 0xea00, 0
	v_add_u32_e32 v159, s26, v157
	v_add_u32_e32 v190, v159, v155
	ds_read2_b64 v[68:71], v190 offset1:2
	ds_read2_b64 v[84:87], v190 offset0:4 offset1:6
	ds_read2_b64 v[88:91], v190 offset0:8 offset1:10
	ds_read2_b64 v[92:95], v190 offset0:12 offset1:14
	ds_read2_b64 v[96:99], v190 offset0:16 offset1:18
	ds_read2_b64 v[100:103], v190 offset0:20 offset1:22
	ds_read2_b64 v[104:107], v190 offset0:24 offset1:26
	ds_read2_b64 v[108:111], v190 offset0:28 offset1:30
	v_add_u32_e32 v112, 0x2000, v190
	v_add_u32_e32 v182, 0x2000, v190
	v_add_u32_e32 v186, 0x2000, v190
	v_add_u32_e32 v214, 0x2000, v190
	ds_read2_b64 v[112:115], v112 offset0:48 offset1:50
	ds_read2_b64 v[182:185], v182 offset0:52 offset1:54
	ds_read2_b64 v[186:189], v186 offset0:56 offset1:58
	ds_read2_b64 v[214:217], v214 offset0:60 offset1:62
	v_cvt_pk_bf16_f32 v116, v52, v53
	v_cvt_pk_bf16_f32 v117, v54, v55
	v_cvt_pk_bf16_f32 v118, v56, v57
	v_cvt_pk_bf16_f32 v119, v58, v59
	v_cvt_pk_bf16_f32 v120, v60, v61
	v_cvt_pk_bf16_f32 v121, v62, v63
	v_cvt_pk_bf16_f32 v122, v64, v65
	v_cvt_pk_bf16_f32 v123, v66, v67
	v_cvt_pk_bf16_f32 v124, v36, v37
	v_cvt_pk_bf16_f32 v125, v38, v39
	v_cvt_pk_bf16_f32 v126, v40, v41
	v_cvt_pk_bf16_f32 v127, v42, v43
	v_cvt_pk_bf16_f32 v128, v44, v45
	v_cvt_pk_bf16_f32 v129, v46, v47
	v_cvt_pk_bf16_f32 v130, v48, v49
	v_cvt_pk_bf16_f32 v131, v50, v51
	v_cvt_pk_bf16_f32 v132, v20, v21
	v_cvt_pk_bf16_f32 v133, v22, v23
	v_cvt_pk_bf16_f32 v134, v24, v25
	v_cvt_pk_bf16_f32 v135, v26, v27
	v_cvt_pk_bf16_f32 v136, v28, v29
	v_cvt_pk_bf16_f32 v137, v30, v31
	v_cvt_pk_bf16_f32 v138, v32, v33
	v_cvt_pk_bf16_f32 v139, v34, v35
	v_cvt_pk_bf16_f32 v140, v4, v5
	v_cvt_pk_bf16_f32 v141, v6, v7
	v_cvt_pk_bf16_f32 v142, v8, v9
	v_cvt_pk_bf16_f32 v143, v10, v11
	v_cvt_pk_bf16_f32 v144, v12, v13
	v_cvt_pk_bf16_f32 v145, v14, v15
	v_cvt_pk_bf16_f32 v146, v16, v17
	v_cvt_pk_bf16_f32 v147, v18, v19
	s_waitcnt lgkmcnt(4)
	v_mfma_f32_32x32x16_bf16 v[68:83], v[68:71], v[116:119], 0
	v_mfma_f32_32x32x16_bf16 v[68:83], v[84:87], v[120:123], v[68:83]
	v_add_u32_e32 v84, 0x2000, v190
	ds_read2_b64 v[84:87], v84 offset0:32 offset1:34
	v_mfma_f32_32x32x16_bf16 v[68:83], v[88:91], v[124:127], v[68:83]
	v_mfma_f32_32x32x16_bf16 v[68:83], v[92:95], v[128:131], v[68:83]
	v_mfma_f32_32x32x16_bf16 v[68:83], v[96:99], v[132:135], v[68:83]
	v_mfma_f32_32x32x16_bf16 v[68:83], v[100:103], v[136:139], v[68:83]
	v_add_u32_e32 v100, 0x2000, v190
	ds_read2_b64 v[100:103], v100 offset0:36 offset1:38
	v_mfma_f32_32x32x16_bf16 v[68:83], v[104:107], v[140:143], v[68:83]
	v_add_u32_e32 v104, 0x2000, v190
	ds_read2_b64 v[104:107], v104 offset0:40 offset1:42
	v_mfma_f32_32x32x16_bf16 v[68:83], v[108:111], v[144:147], v[68:83]
	v_add_u32_e32 v108, 0x2000, v190
	ds_read2_b64 v[108:111], v108 offset0:44 offset1:46
	v_add_u32_e32 v88, 0x2000, v190
	s_waitcnt lgkmcnt(3)
	v_mfma_f32_32x32x16_bf16 v[84:99], v[84:87], v[116:119], 0
	s_waitcnt lgkmcnt(2)
	v_mfma_f32_32x32x16_bf16 v[84:99], v[100:103], v[120:123], v[84:99]
	s_waitcnt lgkmcnt(1)
	v_mfma_f32_32x32x16_bf16 v[84:99], v[104:107], v[124:127], v[84:99]
	s_waitcnt lgkmcnt(0)
	v_mfma_f32_32x32x16_bf16 v[84:99], v[108:111], v[128:131], v[84:99]
	v_mfma_f32_32x32x16_bf16 v[84:99], v[112:115], v[132:135], v[84:99]
	v_mfma_f32_32x32x16_bf16 v[84:99], v[182:185], v[136:139], v[84:99]
	v_mfma_f32_32x32x16_bf16 v[84:99], v[186:189], v[140:143], v[84:99]
	v_mfma_f32_32x32x16_bf16 v[84:99], v[214:217], v[144:147], v[84:99]
	s_waitcnt vmcnt(32)
	v_mov_b32_e32 v200, v201
	v_sub_f32_e32 v81, v197, v81
	v_sub_f32_e32 v80, v196, v80
	v_sub_f32_e32 v71, v165, v71
	v_sub_f32_e32 v70, v164, v70
	v_sub_f32_e32 v69, v167, v69
	v_sub_f32_e32 v68, v166, v68
	v_cvt_pk_bf16_f32 v106, v80, v81
	s_nop 3
	v_sub_f32_e32 v80, v175, v87
	v_sub_f32_e32 v81, v174, v86
	v_sub_f32_e32 v83, v199, v83
	v_sub_f32_e32 v82, v198, v82
	v_sub_f32_e32 v79, v195, v79
	v_sub_f32_e32 v78, v194, v78
	v_sub_f32_e32 v77, v181, v77
	v_sub_f32_e32 v76, v180, v76
	v_sub_f32_e32 v75, v171, v75
	v_sub_f32_e32 v74, v170, v74
	v_sub_f32_e32 v73, v169, v73
	v_sub_f32_e32 v72, v168, v72
	v_cvt_pk_bf16_f32 v100, v68, v69
	v_cvt_pk_bf16_f32 v101, v70, v71
	v_sub_f32_e32 v68, v179, v91
	v_sub_f32_e32 v69, v178, v90
	v_sub_f32_e32 v70, v177, v89
	v_sub_f32_e32 v71, v176, v88
	v_cvt_pk_bf16_f32 v109, v81, v80
	v_add_u32_e32 v80, 0x4000, v190
	v_cvt_pk_bf16_f32 v102, v72, v73
	v_cvt_pk_bf16_f32 v103, v74, v75
	v_cvt_pk_bf16_f32 v104, v76, v77
	v_cvt_pk_bf16_f32 v105, v78, v79
	v_cvt_pk_bf16_f32 v107, v82, v83
	v_sub_f32_e32 v72, v209, v99
	v_sub_f32_e32 v73, v208, v98
	v_sub_f32_e32 v74, v207, v97
	v_sub_f32_e32 v75, v206, v96
	v_sub_f32_e32 v76, v205, v95
	v_sub_f32_e32 v77, v204, v94
	v_sub_f32_e32 v78, v203, v93
	v_sub_f32_e32 v79, v202, v92
	v_sub_f32_e32 v82, v173, v85
	v_sub_f32_e32 v83, v172, v84
	v_cvt_pk_bf16_f32 v110, v71, v70
	v_cvt_pk_bf16_f32 v111, v69, v68
	ds_read2_b64 v[68:71], v80 offset0:64 offset1:66
	ds_read2_b64 v[84:87], v80 offset0:68 offset1:70
	ds_read2_b64 v[88:91], v80 offset0:72 offset1:74
	ds_read2_b64 v[92:95], v80 offset0:76 offset1:78
	ds_read2_b64 v[96:99], v80 offset0:80 offset1:82
	ds_read2_b64 v[164:167], v80 offset0:84 offset1:86
	ds_read2_b64 v[168:171], v80 offset0:88 offset1:90
	ds_read2_b64 v[172:175], v80 offset0:92 offset1:94
	v_add_u32_e32 v176, 0x6000, v190
	v_add_u32_e32 v180, 0x6000, v190
	v_add_u32_e32 v184, 0x6000, v190
	v_add_u32_e32 v194, 0x6000, v190
	ds_read2_b64 v[176:179], v176 offset0:112 offset1:114
	ds_read2_b64 v[180:183], v180 offset0:116 offset1:118
	ds_read2_b64 v[184:187], v184 offset0:120 offset1:122
	ds_read2_b64 v[194:197], v194 offset0:124 offset1:126
	v_cvt_pk_bf16_f32 v108, v83, v82
	v_cvt_pk_bf16_f32 v112, v79, v78
	v_cvt_pk_bf16_f32 v113, v77, v76
	v_cvt_pk_bf16_f32 v114, v75, v74
	v_cvt_pk_bf16_f32 v115, v73, v72
	s_waitcnt lgkmcnt(11)
	v_mfma_f32_32x32x16_bf16 v[68:83], v[68:71], v[116:119], 0
	s_waitcnt lgkmcnt(10)
	v_mfma_f32_32x32x16_bf16 v[68:83], v[84:87], v[120:123], v[68:83]
	v_add_u32_e32 v84, 0x6000, v190
	ds_read2_b64 v[84:87], v84 offset0:96 offset1:98
	s_waitcnt lgkmcnt(10)
	v_mfma_f32_32x32x16_bf16 v[68:83], v[88:91], v[124:127], v[68:83]
	s_waitcnt lgkmcnt(9)
	v_mfma_f32_32x32x16_bf16 v[68:83], v[92:95], v[128:131], v[68:83]
	s_waitcnt lgkmcnt(8)
	v_mfma_f32_32x32x16_bf16 v[68:83], v[96:99], v[132:135], v[68:83]
	s_waitcnt lgkmcnt(7)
	v_mfma_f32_32x32x16_bf16 v[68:83], v[164:167], v[136:139], v[68:83]
	v_add_u32_e32 v164, 0x6000, v190
	ds_read2_b64 v[164:167], v164 offset0:100 offset1:102
	s_waitcnt lgkmcnt(7)
	v_mfma_f32_32x32x16_bf16 v[68:83], v[168:171], v[140:143], v[68:83]
	v_add_u32_e32 v168, 0x6000, v190
	ds_read2_b64 v[168:171], v168 offset0:104 offset1:106
	s_waitcnt lgkmcnt(7)
	v_mfma_f32_32x32x16_bf16 v[68:83], v[172:175], v[144:147], v[68:83]
	v_add_u32_e32 v172, 0x6000, v190
	ds_read2_b64 v[172:175], v172 offset0:108 offset1:110
	v_add_u32_e32 v88, 0x6000, v190
	s_waitcnt lgkmcnt(3)
	v_mfma_f32_32x32x16_bf16 v[84:99], v[84:87], v[116:119], 0
	v_add_u32_e32 v116, v159, v153
	v_add_u32_e32 v116, 0x8000, v116
	ds_read2_b64 v[116:119], v116 offset0:128 offset1:130
	s_waitcnt lgkmcnt(3)
	v_mfma_f32_32x32x16_bf16 v[84:99], v[164:167], v[120:123], v[84:99]
	v_add_u32_e32 v120, v159, v153
	v_add_u32_e32 v120, 0x8000, v120
	ds_read2_b64 v[120:123], v120 offset0:132 offset1:134
	s_waitcnt lgkmcnt(3)
	v_mfma_f32_32x32x16_bf16 v[84:99], v[168:171], v[124:127], v[84:99]
	v_add_u32_e32 v124, v159, v153
	v_add_u32_e32 v124, 0x8000, v124
	ds_read2_b64 v[124:127], v124 offset0:136 offset1:138
	s_waitcnt lgkmcnt(3)
	v_mfma_f32_32x32x16_bf16 v[84:99], v[172:175], v[128:131], v[84:99]
	v_add_u32_e32 v128, v159, v153
	v_add_u32_e32 v128, 0x8000, v128
	ds_read2_b64 v[128:131], v128 offset0:140 offset1:142
	v_mfma_f32_32x32x16_bf16 v[84:99], v[176:179], v[132:135], v[84:99]
	v_add_u32_e32 v132, v159, v153
	v_add_u32_e32 v132, 0x9000, v132
	ds_read2_b64 v[132:135], v132 offset0:160 offset1:162
	v_mfma_f32_32x32x16_bf16 v[84:99], v[180:183], v[136:139], v[84:99]
	v_add_u32_e32 v136, v159, v153
	v_add_u32_e32 v136, 0x9000, v136
	ds_read2_b64 v[136:139], v136 offset0:164 offset1:166
	v_mfma_f32_32x32x16_bf16 v[84:99], v[184:187], v[140:143], v[84:99]
	v_add_u32_e32 v140, v159, v153
	v_add_u32_e32 v140, 0x9000, v140
	ds_read2_b64 v[140:143], v140 offset0:168 offset1:170
	v_mfma_f32_32x32x16_bf16 v[84:99], v[194:197], v[144:147], v[84:99]
	v_add_u32_e32 v144, v159, v153
	v_add_u32_e32 v144, 0x9000, v144
	ds_read2_b64 v[144:147], v144 offset0:172 offset1:174
	v_add_u32_e32 v159, v159, v153
	v_lshl_add_u64 v[182:183], s[6:7], 0, v[162:163]
	s_add_i32 s35, s35, 1
	s_add_u32 s26, s6, s28
	s_addc_u32 s27, s7, s29
	v_mov_b64_e32 v[232:233], s[26:27]
	global_load_dword v201, v[232:233], off
	s_waitcnt lgkmcnt(7)
	v_mfma_f32_32x32x16_bf16 v[68:83], v[116:119], v[100:103], v[68:83]
	s_mov_b32 s26, 0x41a20000
	v_add_co_u32_e32 v218, vcc, s26, v182
	s_nop 1
	v_addc_co_u32_e32 v219, vcc, 0, v183, vcc
	s_mov_b32 s26, 0x41a21000
	v_add_co_u32_e32 v220, vcc, s26, v182
	s_nop 1
	v_addc_co_u32_e32 v221, vcc, 0, v183, vcc
	global_load_dword v166, v[218:219], off
	global_load_dword v167, v[218:219], off offset:2048
	global_load_dword v164, v[220:221], off
	global_load_dword v165, v[220:221], off offset:2048
	s_waitcnt lgkmcnt(3)
	v_mfma_f32_32x32x16_bf16 v[84:99], v[132:135], v[100:103], v[84:99]
	s_mov_b32 s26, 0x41a24000
	v_add_co_u32_e32 v222, vcc, s26, v182
	s_nop 1
	v_addc_co_u32_e32 v223, vcc, 0, v183, vcc
	s_mov_b32 s26, 0x41a25000
	v_add_co_u32_e32 v224, vcc, s26, v182
	s_nop 1
	v_addc_co_u32_e32 v225, vcc, 0, v183, vcc
	global_load_dword v168, v[222:223], off
	global_load_dword v169, v[222:223], off offset:2048
	global_load_dword v170, v[224:225], off
	global_load_dword v171, v[224:225], off offset:2048
	v_mfma_f32_32x32x16_bf16 v[68:83], v[120:123], v[104:107], v[68:83]
	s_mov_b32 s26, 0x41a28000
	v_add_co_u32_e32 v218, vcc, s26, v182
	s_nop 1
	v_addc_co_u32_e32 v219, vcc, 0, v183, vcc
	s_mov_b32 s26, 0x41a29000
	v_add_co_u32_e32 v220, vcc, s26, v182
	s_nop 1
	v_addc_co_u32_e32 v221, vcc, 0, v183, vcc
	global_load_dword v180, v[218:219], off
	global_load_dword v181, v[218:219], off offset:2048
	global_load_dword v194, v[220:221], off
	global_load_dword v195, v[220:221], off offset:2048
	s_waitcnt lgkmcnt(2)
	v_mfma_f32_32x32x16_bf16 v[84:99], v[136:139], v[104:107], v[84:99]
	s_mov_b32 s26, 0x41a2c000
	v_add_co_u32_e32 v222, vcc, s26, v182
	s_nop 1
	v_addc_co_u32_e32 v223, vcc, 0, v183, vcc
	s_mov_b32 s26, 0x41a2d000
	v_add_co_u32_e32 v224, vcc, s26, v182
	s_nop 1
	v_addc_co_u32_e32 v225, vcc, 0, v183, vcc
	global_load_dword v196, v[222:223], off
	global_load_dword v197, v[222:223], off offset:2048
	global_load_dword v198, v[224:225], off
	global_load_dword v199, v[224:225], off offset:2048
	v_mfma_f32_32x32x16_bf16 v[68:83], v[124:127], v[108:111], v[68:83]
	s_mov_b32 s26, 0x41a30000
	v_add_co_u32_e32 v218, vcc, s26, v182
	s_nop 1
	v_addc_co_u32_e32 v219, vcc, 0, v183, vcc
	s_mov_b32 s26, 0x41a31000
	v_add_co_u32_e32 v220, vcc, s26, v182
	s_nop 1
	v_addc_co_u32_e32 v221, vcc, 0, v183, vcc
	global_load_dword v172, v[218:219], off
	global_load_dword v173, v[218:219], off offset:2048
	global_load_dword v174, v[220:221], off
	global_load_dword v175, v[220:221], off offset:2048
	s_waitcnt lgkmcnt(1)
	v_mfma_f32_32x32x16_bf16 v[84:99], v[140:143], v[108:111], v[84:99]
	s_mov_b32 s26, 0x41a34000
	v_add_co_u32_e32 v222, vcc, s26, v182
	s_nop 1
	v_addc_co_u32_e32 v223, vcc, 0, v183, vcc
	s_mov_b32 s26, 0x41a35000
	v_add_co_u32_e32 v224, vcc, s26, v182
	s_nop 1
	v_addc_co_u32_e32 v225, vcc, 0, v183, vcc
	global_load_dword v176, v[222:223], off
	global_load_dword v177, v[222:223], off offset:2048
	global_load_dword v178, v[224:225], off
	global_load_dword v179, v[224:225], off offset:2048
	v_mfma_f32_32x32x16_bf16 v[68:83], v[128:131], v[112:115], v[68:83]
	s_mov_b32 s26, 0x41a38000
	v_add_co_u32_e32 v218, vcc, s26, v182
	s_nop 1
	v_addc_co_u32_e32 v219, vcc, 0, v183, vcc
	s_mov_b32 s26, 0x41a39000
	v_add_co_u32_e32 v220, vcc, s26, v182
	s_nop 1
	v_addc_co_u32_e32 v221, vcc, 0, v183, vcc
	global_load_dword v202, v[218:219], off
	global_load_dword v203, v[218:219], off offset:2048
	global_load_dword v204, v[220:221], off
	global_load_dword v205, v[220:221], off offset:2048
	s_waitcnt lgkmcnt(0)
	v_mfma_f32_32x32x16_bf16 v[84:99], v[144:147], v[112:115], v[84:99]
	s_mov_b32 s26, 0x41a3c000
	v_add_co_u32_e32 v222, vcc, s26, v182
	s_nop 1
	v_addc_co_u32_e32 v223, vcc, 0, v183, vcc
	s_mov_b32 s26, 0x41a3d000
	v_add_co_u32_e32 v224, vcc, s26, v182
	s_nop 1
	v_addc_co_u32_e32 v225, vcc, 0, v183, vcc
	global_load_dword v206, v[222:223], off
	global_load_dword v207, v[222:223], off offset:2048
	global_load_dword v208, v[224:225], off
	global_load_dword v209, v[224:225], off offset:2048
	v_add_u32_e32 v116, 0xa000, v159
	ds_read2_b64 v[116:119], v116 offset0:192 offset1:194
	v_add_u32_e32 v120, 0xa000, v159
	ds_read2_b64 v[120:123], v120 offset0:196 offset1:198
	v_add_u32_e32 v124, 0xa000, v159
	ds_read2_b64 v[124:127], v124 offset0:200 offset1:202
	v_add_u32_e32 v128, 0xa000, v159
	ds_read2_b64 v[128:131], v128 offset0:204 offset1:206
	v_add_u32_e32 v132, 0xb000, v159
	ds_read2_b64 v[132:135], v132 offset0:224 offset1:226
	v_add_u32_e32 v136, 0xb000, v159
	ds_read2_b64 v[136:139], v136 offset0:228 offset1:230
	v_add_u32_e32 v140, 0xb000, v159
	ds_read2_b64 v[140:143], v140 offset0:232 offset1:234
	v_add_u32_e32 v144, 0xb000, v159
	ds_read2_b64 v[144:147], v144 offset0:236 offset1:238
	v_pk_mul_f32 v[66:67], v[66:67], v[200:201] op_sel_hi:[1,0]
	v_pk_mul_f32 v[64:65], v[64:65], v[200:201] op_sel_hi:[1,0]
	v_pk_mul_f32 v[62:63], v[62:63], v[200:201] op_sel_hi:[1,0]
	v_pk_mul_f32 v[60:61], v[60:61], v[200:201] op_sel_hi:[1,0]
	v_pk_mul_f32 v[58:59], v[58:59], v[200:201] op_sel_hi:[1,0]
	v_pk_mul_f32 v[56:57], v[56:57], v[200:201] op_sel_hi:[1,0]
	v_pk_mul_f32 v[54:55], v[54:55], v[200:201] op_sel_hi:[1,0]
	v_pk_mul_f32 v[52:53], v[52:53], v[200:201] op_sel_hi:[1,0]
	v_pk_mul_f32 v[50:51], v[50:51], v[200:201] op_sel_hi:[1,0]
	v_pk_mul_f32 v[48:49], v[48:49], v[200:201] op_sel_hi:[1,0]
	v_pk_mul_f32 v[46:47], v[46:47], v[200:201] op_sel_hi:[1,0]
	v_pk_mul_f32 v[44:45], v[44:45], v[200:201] op_sel_hi:[1,0]
	v_pk_mul_f32 v[42:43], v[42:43], v[200:201] op_sel_hi:[1,0]
	v_pk_mul_f32 v[40:41], v[40:41], v[200:201] op_sel_hi:[1,0]
	v_pk_mul_f32 v[38:39], v[38:39], v[200:201] op_sel_hi:[1,0]
	v_pk_mul_f32 v[36:37], v[36:37], v[200:201] op_sel_hi:[1,0]
	s_waitcnt lgkmcnt(0)
	v_mfma_f32_32x32x16_bf16 v[52:67], v[116:119], v[100:103], v[52:67]
	s_mov_b32 s26, 0x47200000
	v_add_co_u32_e32 v218, vcc, s26, v182
	s_nop 1
	v_addc_co_u32_e32 v219, vcc, 0, v183, vcc
	global_store_dword v[218:219], v68, off
	global_store_dword v[218:219], v69, off offset:2048
	v_mfma_f32_32x32x16_bf16 v[36:51], v[132:135], v[100:103], v[36:51]
	s_mov_b32 s26, 0x47201000
	v_add_co_u32_e32 v220, vcc, s26, v182
	s_nop 1
	v_addc_co_u32_e32 v221, vcc, 0, v183, vcc
	global_store_dword v[220:221], v70, off
	global_store_dword v[220:221], v71, off offset:2048
	v_mfma_f32_32x32x16_bf16 v[52:67], v[120:123], v[104:107], v[52:67]
	s_mov_b32 s26, 0x47204000
	v_add_co_u32_e32 v222, vcc, s26, v182
	s_nop 1
	v_addc_co_u32_e32 v223, vcc, 0, v183, vcc
	global_store_dword v[222:223], v72, off
	global_store_dword v[222:223], v73, off offset:2048
	v_mfma_f32_32x32x16_bf16 v[36:51], v[136:139], v[104:107], v[36:51]
	s_mov_b32 s26, 0x47205000
	v_add_co_u32_e32 v224, vcc, s26, v182
	s_nop 1
	v_addc_co_u32_e32 v225, vcc, 0, v183, vcc
	global_store_dword v[224:225], v74, off
	global_store_dword v[224:225], v75, off offset:2048
	v_mfma_f32_32x32x16_bf16 v[52:67], v[124:127], v[108:111], v[52:67]
	s_mov_b32 s26, 0x47208000
	v_add_co_u32_e32 v218, vcc, s26, v182
	s_nop 1
	v_addc_co_u32_e32 v219, vcc, 0, v183, vcc
	global_store_dword v[218:219], v76, off
	global_store_dword v[218:219], v77, off offset:2048
	v_mfma_f32_32x32x16_bf16 v[36:51], v[140:143], v[108:111], v[36:51]
	s_mov_b32 s26, 0x47209000
	v_add_co_u32_e32 v220, vcc, s26, v182
	s_nop 1
	v_addc_co_u32_e32 v221, vcc, 0, v183, vcc
	global_store_dword v[220:221], v78, off
	global_store_dword v[220:221], v79, off offset:2048
	v_mfma_f32_32x32x16_bf16 v[52:67], v[128:131], v[112:115], v[52:67]
	s_mov_b32 s26, 0x4720c000
	v_add_co_u32_e32 v222, vcc, s26, v182
	s_nop 1
	v_addc_co_u32_e32 v223, vcc, 0, v183, vcc
	global_store_dword v[222:223], v80, off
	global_store_dword v[222:223], v81, off offset:2048
	v_mfma_f32_32x32x16_bf16 v[36:51], v[144:147], v[112:115], v[36:51]
	s_mov_b32 s26, 0x4720d000
	v_add_co_u32_e32 v224, vcc, s26, v182
	s_nop 1
	v_addc_co_u32_e32 v225, vcc, 0, v183, vcc
	global_store_dword v[224:225], v82, off
	global_store_dword v[224:225], v83, off offset:2048
	v_add_u32_e32 v116, 0xc800, v159
	ds_read2_b64 v[116:119], v116 offset1:2
	v_add_u32_e32 v120, 0xc800, v159
	ds_read2_b64 v[120:123], v120 offset0:4 offset1:6
	v_add_u32_e32 v124, 0xc800, v159
	ds_read2_b64 v[124:127], v124 offset0:8 offset1:10
	v_add_u32_e32 v128, 0xc800, v159
	ds_read2_b64 v[128:131], v128 offset0:12 offset1:14
	v_add_u32_e32 v132, 0xd800, v159
	ds_read2_b64 v[132:135], v132 offset0:32 offset1:34
	v_add_u32_e32 v136, 0xd800, v159
	ds_read2_b64 v[136:139], v136 offset0:36 offset1:38
	v_add_u32_e32 v140, 0xd800, v159
	ds_read2_b64 v[140:143], v140 offset0:40 offset1:42
	v_add_u32_e32 v144, 0xd800, v159
	ds_read2_b64 v[144:147], v144 offset0:44 offset1:46
	v_pk_mul_f32 v[34:35], v[34:35], v[200:201] op_sel_hi:[1,0]
	v_pk_mul_f32 v[32:33], v[32:33], v[200:201] op_sel_hi:[1,0]
	v_pk_mul_f32 v[30:31], v[30:31], v[200:201] op_sel_hi:[1,0]
	v_pk_mul_f32 v[28:29], v[28:29], v[200:201] op_sel_hi:[1,0]
	v_pk_mul_f32 v[26:27], v[26:27], v[200:201] op_sel_hi:[1,0]
	v_pk_mul_f32 v[24:25], v[24:25], v[200:201] op_sel_hi:[1,0]
	v_pk_mul_f32 v[22:23], v[22:23], v[200:201] op_sel_hi:[1,0]
	v_pk_mul_f32 v[20:21], v[20:21], v[200:201] op_sel_hi:[1,0]
	v_pk_mul_f32 v[18:19], v[18:19], v[200:201] op_sel_hi:[1,0]
	v_pk_mul_f32 v[16:17], v[16:17], v[200:201] op_sel_hi:[1,0]
	v_pk_mul_f32 v[14:15], v[14:15], v[200:201] op_sel_hi:[1,0]
	v_pk_mul_f32 v[12:13], v[12:13], v[200:201] op_sel_hi:[1,0]
	v_pk_mul_f32 v[10:11], v[10:11], v[200:201] op_sel_hi:[1,0]
	v_pk_mul_f32 v[8:9], v[8:9], v[200:201] op_sel_hi:[1,0]
	v_pk_mul_f32 v[6:7], v[6:7], v[200:201] op_sel_hi:[1,0]
	v_pk_mul_f32 v[4:5], v[4:5], v[200:201] op_sel_hi:[1,0]
	s_waitcnt lgkmcnt(0)
	v_mfma_f32_32x32x16_bf16 v[20:35], v[116:119], v[100:103], v[20:35]
	s_mov_b32 s26, 0x47210000
	v_add_co_u32_e32 v218, vcc, s26, v182
	s_nop 1
	v_addc_co_u32_e32 v219, vcc, 0, v183, vcc
	global_store_dword v[218:219], v84, off
	global_store_dword v[218:219], v85, off offset:2048
	v_mfma_f32_32x32x16_bf16 v[4:19], v[132:135], v[100:103], v[4:19]
	s_mov_b32 s26, 0x47211000
	v_add_co_u32_e32 v220, vcc, s26, v182
	s_nop 1
	v_addc_co_u32_e32 v221, vcc, 0, v183, vcc
	global_store_dword v[220:221], v86, off
	global_store_dword v[220:221], v87, off offset:2048
	v_mfma_f32_32x32x16_bf16 v[20:35], v[120:123], v[104:107], v[20:35]
	s_mov_b32 s26, 0x47214000
	v_add_co_u32_e32 v222, vcc, s26, v182
	s_nop 1
	v_addc_co_u32_e32 v223, vcc, 0, v183, vcc
	global_store_dword v[222:223], v88, off
	global_store_dword v[222:223], v89, off offset:2048
	v_mfma_f32_32x32x16_bf16 v[4:19], v[136:139], v[104:107], v[4:19]
	s_mov_b32 s26, 0x47215000
	v_add_co_u32_e32 v224, vcc, s26, v182
	s_nop 1
	v_addc_co_u32_e32 v225, vcc, 0, v183, vcc
	global_store_dword v[224:225], v90, off
	global_store_dword v[224:225], v91, off offset:2048
	v_mfma_f32_32x32x16_bf16 v[20:35], v[124:127], v[108:111], v[20:35]
	s_mov_b32 s26, 0x47218000
	v_add_co_u32_e32 v218, vcc, s26, v182
	s_nop 1
	v_addc_co_u32_e32 v219, vcc, 0, v183, vcc
	global_store_dword v[218:219], v92, off
	global_store_dword v[218:219], v93, off offset:2048
	v_mfma_f32_32x32x16_bf16 v[4:19], v[140:143], v[108:111], v[4:19]
	s_mov_b32 s26, 0x47219000
	v_add_co_u32_e32 v220, vcc, s26, v182
	s_nop 1
	v_addc_co_u32_e32 v221, vcc, 0, v183, vcc
	global_store_dword v[220:221], v94, off
	global_store_dword v[220:221], v95, off offset:2048
	v_mfma_f32_32x32x16_bf16 v[20:35], v[128:131], v[112:115], v[20:35]
	s_mov_b32 s26, 0x4721c000
	v_add_co_u32_e32 v222, vcc, s26, v182
	s_nop 1
	v_addc_co_u32_e32 v223, vcc, 0, v183, vcc
	global_store_dword v[222:223], v96, off
	global_store_dword v[222:223], v97, off offset:2048
	v_mfma_f32_32x32x16_bf16 v[4:19], v[144:147], v[112:115], v[4:19]
	s_mov_b32 s26, 0x4721d000
	v_add_co_u32_e32 v224, vcc, s26, v182
	s_nop 1
	v_addc_co_u32_e32 v225, vcc, 0, v183, vcc
	global_store_dword v[224:225], v98, off
	global_store_dword v[224:225], v99, off offset:2048
	s_add_u32 s28, s28, 4
	s_addc_u32 s29, s29, 0
	v_lshl_add_u64 v[162:163], v[162:163], 0, s[38:39]
	s_cmp_eq_u32 s35, 63
	s_barrier
	s_cbranch_scc0 .LBB0_490
	s_waitcnt vmcnt(32)
	v_add_u32_e32 v82, v157, v155
	v_cvt_pk_bf16_f32 v52, v52, v53
	v_cvt_pk_bf16_f32 v53, v54, v55
	v_cvt_pk_bf16_f32 v54, v56, v57
	v_cvt_pk_bf16_f32 v57, v62, v63
	v_cvt_pk_bf16_f32 v62, v8, v9
	v_add_u32_e32 v8, 0xe800, v82
	v_cvt_pk_bf16_f32 v56, v60, v61
	v_cvt_pk_bf16_f32 v36, v36, v37
	v_cvt_pk_bf16_f32 v37, v38, v39
	v_cvt_pk_bf16_f32 v38, v40, v41
	v_cvt_pk_bf16_f32 v39, v42, v43
	v_cvt_pk_bf16_f32 v40, v44, v45
	v_cvt_pk_bf16_f32 v41, v46, v47
	v_cvt_pk_bf16_f32 v42, v48, v49
	v_cvt_pk_bf16_f32 v43, v50, v51
	v_cvt_pk_bf16_f32 v44, v20, v21
	v_cvt_pk_bf16_f32 v45, v22, v23
	v_cvt_pk_bf16_f32 v46, v24, v25
	v_cvt_pk_bf16_f32 v47, v26, v27
	v_cvt_pk_bf16_f32 v48, v28, v29
	v_cvt_pk_bf16_f32 v49, v30, v31
	v_cvt_pk_bf16_f32 v50, v32, v33
	v_cvt_pk_bf16_f32 v51, v34, v35
	v_cvt_pk_bf16_f32 v60, v4, v5
	v_cvt_pk_bf16_f32 v61, v6, v7
	ds_read2_b64 v[4:7], v8 offset0:64 offset1:66
	ds_read2_b64 v[20:23], v8 offset0:68 offset1:70
	ds_read2_b64 v[24:27], v8 offset0:72 offset1:74
	ds_read2_b64 v[28:31], v8 offset0:76 offset1:78
	ds_read2_b64 v[32:35], v8 offset0:80 offset1:82
	ds_read2_b64 v[68:71], v8 offset0:84 offset1:86
	ds_read2_b64 v[72:75], v8 offset0:88 offset1:90
	ds_read2_b64 v[78:81], v8 offset0:92 offset1:94
	s_add_u32 s24, s6, s24
	s_addc_u32 s25, s7, s25
	s_add_u32 s24, s24, s9
	s_addc_u32 s25, s25, 0
	v_lshl_add_u64 v[76:77], v[160:161], 2, s[24:25]
	v_cvt_pk_bf16_f32 v55, v58, v59
	v_cvt_pk_bf16_f32 v58, v64, v65
	v_cvt_pk_bf16_f32 v59, v66, v67
	v_cvt_pk_bf16_f32 v63, v10, v11
	v_cvt_pk_bf16_f32 v64, v12, v13
	v_cvt_pk_bf16_f32 v65, v14, v15
	v_cvt_pk_bf16_f32 v66, v16, v17
	v_cvt_pk_bf16_f32 v67, v18, v19
	s_waitcnt lgkmcnt(7)
	v_mfma_f32_32x32x16_bf16 v[4:19], v[4:7], v[52:55], 0
	s_waitcnt lgkmcnt(6)
	v_mfma_f32_32x32x16_bf16 v[4:19], v[20:23], v[56:59], v[4:19]
	s_waitcnt lgkmcnt(5)
	v_mfma_f32_32x32x16_bf16 v[4:19], v[24:27], v[36:39], v[4:19]
	s_waitcnt lgkmcnt(4)
	v_mfma_f32_32x32x16_bf16 v[4:19], v[28:31], v[40:43], v[4:19]
	s_waitcnt lgkmcnt(3)
	v_mfma_f32_32x32x16_bf16 v[4:19], v[32:35], v[44:47], v[4:19]
	s_waitcnt lgkmcnt(2)
	v_mfma_f32_32x32x16_bf16 v[4:19], v[68:71], v[48:51], v[4:19]
	s_waitcnt lgkmcnt(1)
	v_mfma_f32_32x32x16_bf16 v[4:19], v[72:75], v[60:63], v[4:19]
	s_waitcnt lgkmcnt(0)
	v_mfma_f32_32x32x16_bf16 v[4:19], v[78:81], v[64:67], v[4:19]
	v_add_u32_e32 v20, 0x2100, v82
	v_add_u32_e32 v24, 0xe800, v20
	ds_read2_b64 v[20:23], v24 offset0:64 offset1:66
	ds_read2_b64 v[68:71], v24 offset0:68 offset1:70
	ds_read2_b64 v[72:75], v24 offset0:72 offset1:74
	ds_read2_b64 v[78:81], v24 offset0:76 offset1:78
	ds_read2_b64 v[82:85], v24 offset0:80 offset1:82
	ds_read2_b64 v[86:89], v24 offset0:84 offset1:86
	ds_read2_b64 v[90:93], v24 offset0:88 offset1:90
	ds_read2_b64 v[94:97], v24 offset0:92 offset1:94
	s_waitcnt lgkmcnt(7)
	v_mfma_f32_32x32x16_bf16 v[20:35], v[20:23], v[52:55], 0
	s_waitcnt lgkmcnt(6)
	v_mfma_f32_32x32x16_bf16 v[20:35], v[68:71], v[56:59], v[20:35]
	s_waitcnt lgkmcnt(5)
	v_mfma_f32_32x32x16_bf16 v[20:35], v[72:75], v[36:39], v[20:35]
	s_waitcnt lgkmcnt(4)
	v_mfma_f32_32x32x16_bf16 v[20:35], v[78:81], v[40:43], v[20:35]
	s_waitcnt lgkmcnt(3)
	v_mfma_f32_32x32x16_bf16 v[20:35], v[82:85], v[44:47], v[20:35]
	s_waitcnt lgkmcnt(2)
	v_mfma_f32_32x32x16_bf16 v[20:35], v[86:89], v[48:51], v[20:35]
	s_waitcnt lgkmcnt(1)
	v_mfma_f32_32x32x16_bf16 v[20:35], v[90:93], v[60:63], v[20:35]
	s_waitcnt lgkmcnt(0)
	v_mfma_f32_32x32x16_bf16 v[20:35], v[94:97], v[64:67], v[20:35]
	v_add_f32_e64 v4, v166, -v4
	v_add_f32_e64 v5, v167, -v5
	v_add_f32_e64 v6, v164, -v6
	v_add_f32_e64 v7, v165, -v7
	v_add_f32_e64 v8, v168, -v8
	v_add_f32_e64 v9, v169, -v9
	v_pk_add_f32 v[10:11], v[170:171], v[10:11] neg_lo:[0,1] neg_hi:[0,1]
	v_pk_add_f32 v[12:13], v[180:181], v[12:13] neg_lo:[0,1] neg_hi:[0,1]
	v_pk_add_f32 v[14:15], v[194:195], v[14:15] neg_lo:[0,1] neg_hi:[0,1]
	v_pk_add_f32 v[16:17], v[196:197], v[16:17] neg_lo:[0,1] neg_hi:[0,1]
	v_pk_add_f32 v[18:19], v[198:199], v[18:19] neg_lo:[0,1] neg_hi:[0,1]
	v_cvt_pk_bf16_f32 v68, v4, v5
	v_cvt_pk_bf16_f32 v69, v6, v7
	v_pk_add_f32 v[4:5], v[172:173], v[20:21] neg_lo:[0,1] neg_hi:[0,1]
	v_pk_add_f32 v[6:7], v[174:175], v[22:23] neg_lo:[0,1] neg_hi:[0,1]
	v_add3_u32 v98, s31, v149, v155
	v_cvt_pk_bf16_f32 v70, v8, v9
	v_cvt_pk_bf16_f32 v71, v10, v11
	v_cvt_pk_bf16_f32 v72, v12, v13
	v_cvt_pk_bf16_f32 v73, v14, v15
	v_cvt_pk_bf16_f32 v74, v16, v17
	v_cvt_pk_bf16_f32 v75, v18, v19
	v_pk_add_f32 v[8:9], v[176:177], v[24:25] neg_lo:[0,1] neg_hi:[0,1]
	v_pk_add_f32 v[10:11], v[178:179], v[26:27] neg_lo:[0,1] neg_hi:[0,1]
	v_pk_add_f32 v[12:13], v[202:203], v[28:29] neg_lo:[0,1] neg_hi:[0,1]
	v_pk_add_f32 v[14:15], v[204:205], v[30:31] neg_lo:[0,1] neg_hi:[0,1]
	v_pk_add_f32 v[16:17], v[206:207], v[32:33] neg_lo:[0,1] neg_hi:[0,1]
	v_pk_add_f32 v[18:19], v[208:209], v[34:35] neg_lo:[0,1] neg_hi:[0,1]
	v_cvt_pk_bf16_f32 v78, v4, v5
	v_cvt_pk_bf16_f32 v79, v6, v7
	ds_read2_b64 v[4:7], v98 offset1:2
	ds_read2_b64 v[20:23], v98 offset0:4 offset1:6
	ds_read2_b64 v[24:27], v98 offset0:8 offset1:10
	ds_read2_b64 v[28:31], v98 offset0:12 offset1:14
	ds_read2_b64 v[32:35], v98 offset0:16 offset1:18
	ds_read2_b64 v[82:85], v98 offset0:20 offset1:22
	ds_read2_b64 v[86:89], v98 offset0:24 offset1:26
	ds_read2_b64 v[90:93], v98 offset0:28 offset1:30
	v_cvt_pk_bf16_f32 v80, v8, v9
	v_cvt_pk_bf16_f32 v81, v10, v11
	v_cvt_pk_bf16_f32 v94, v12, v13
	v_cvt_pk_bf16_f32 v95, v14, v15
	v_cvt_pk_bf16_f32 v96, v16, v17
	v_cvt_pk_bf16_f32 v97, v18, v19
	s_waitcnt lgkmcnt(7)
	v_mfma_f32_32x32x16_bf16 v[4:19], v[4:7], v[52:55], 0
	s_waitcnt lgkmcnt(6)
	v_mfma_f32_32x32x16_bf16 v[4:19], v[20:23], v[56:59], v[4:19]
	s_waitcnt lgkmcnt(5)
	v_mfma_f32_32x32x16_bf16 v[4:19], v[24:27], v[36:39], v[4:19]
	s_waitcnt lgkmcnt(4)
	v_mfma_f32_32x32x16_bf16 v[4:19], v[28:31], v[40:43], v[4:19]
	s_waitcnt lgkmcnt(3)
	v_mfma_f32_32x32x16_bf16 v[4:19], v[32:35], v[44:47], v[4:19]
	s_waitcnt lgkmcnt(2)
	v_mfma_f32_32x32x16_bf16 v[4:19], v[82:85], v[48:51], v[4:19]
	s_waitcnt lgkmcnt(1)
	v_mfma_f32_32x32x16_bf16 v[4:19], v[86:89], v[60:63], v[4:19]
	s_waitcnt lgkmcnt(0)
	v_mfma_f32_32x32x16_bf16 v[4:19], v[90:93], v[64:67], v[4:19]
	v_add_u32_e32 v24, 0x2000, v98
	ds_read2_b64 v[20:23], v24 offset0:32 offset1:34
	ds_read2_b64 v[82:85], v24 offset0:36 offset1:38
	ds_read2_b64 v[86:89], v24 offset0:40 offset1:42
	ds_read2_b64 v[90:93], v24 offset0:44 offset1:46
	ds_read2_b64 v[98:101], v24 offset0:48 offset1:50
	ds_read2_b64 v[102:105], v24 offset0:52 offset1:54
	ds_read2_b64 v[106:109], v24 offset0:56 offset1:58
	ds_read2_b64 v[110:113], v24 offset0:60 offset1:62
	s_waitcnt lgkmcnt(7)
	v_mfma_f32_32x32x16_bf16 v[20:35], v[20:23], v[52:55], 0
	s_waitcnt lgkmcnt(6)
	v_mfma_f32_32x32x16_bf16 v[20:35], v[82:85], v[56:59], v[20:35]
	s_waitcnt lgkmcnt(5)
	v_mfma_f32_32x32x16_bf16 v[20:35], v[86:89], v[36:39], v[20:35]
	s_waitcnt lgkmcnt(4)
	v_mfma_f32_32x32x16_bf16 v[20:35], v[90:93], v[40:43], v[20:35]
	s_waitcnt lgkmcnt(3)
	v_mfma_f32_32x32x16_bf16 v[20:35], v[98:101], v[44:47], v[20:35]
	s_waitcnt lgkmcnt(2)
	v_mfma_f32_32x32x16_bf16 v[20:35], v[102:105], v[48:51], v[20:35]
	s_waitcnt lgkmcnt(1)
	v_mfma_f32_32x32x16_bf16 v[20:35], v[106:109], v[60:63], v[20:35]
	s_waitcnt lgkmcnt(0)
	v_mfma_f32_32x32x16_bf16 v[20:35], v[110:113], v[64:67], v[20:35]
	v_add3_u32 v52, s33, v149, v153
	v_add_u32_e32 v64, 0x1000, v52
	ds_read2_b64 v[36:39], v52 offset1:2
	ds_read2_b64 v[40:43], v52 offset0:4 offset1:6
	ds_read2_b64 v[44:47], v52 offset0:8 offset1:10
	ds_read2_b64 v[48:51], v52 offset0:12 offset1:14
	ds_read2_b64 v[52:55], v64 offset0:32 offset1:34
	ds_read2_b64 v[56:59], v64 offset0:36 offset1:38
	ds_read2_b64 v[60:63], v64 offset0:40 offset1:42
	ds_read2_b64 v[64:67], v64 offset0:44 offset1:46
	s_waitcnt lgkmcnt(7)
	v_mfma_f32_32x32x16_bf16 v[4:19], v[36:39], v[68:71], v[4:19]
	s_waitcnt lgkmcnt(3)
	v_mfma_f32_32x32x16_bf16 v[20:35], v[52:55], v[68:71], v[20:35]
	v_mfma_f32_32x32x16_bf16 v[4:19], v[40:43], v[72:75], v[4:19]
	s_waitcnt lgkmcnt(2)
	v_mfma_f32_32x32x16_bf16 v[20:35], v[56:59], v[72:75], v[20:35]
	v_mfma_f32_32x32x16_bf16 v[4:19], v[44:47], v[78:81], v[4:19]
	s_waitcnt lgkmcnt(1)
	v_mfma_f32_32x32x16_bf16 v[20:35], v[60:63], v[78:81], v[20:35]
	v_mfma_f32_32x32x16_bf16 v[4:19], v[48:51], v[94:97], v[4:19]
	s_waitcnt lgkmcnt(0)
	v_mfma_f32_32x32x16_bf16 v[20:35], v[64:67], v[94:97], v[20:35]
	v_lshl_add_u64 v[36:37], v[76:77], 0, v[2:3]
	s_mov_b32 s9, 0x479e0000
	v_add_co_u32_e32 v38, vcc, s9, v36
	s_mov_b32 s9, 0x479e1000
	s_nop 0
	v_addc_co_u32_e32 v39, vcc, 0, v37, vcc
	s_nop 3
	global_store_dword v[38:39], v4, off
	global_store_dword v[38:39], v5, off offset:2048
	v_add_co_u32_e32 v4, vcc, s9, v36
	s_mov_b32 s9, 0x479e4000
	s_nop 0
	v_addc_co_u32_e32 v5, vcc, 0, v37, vcc
	global_store_dword v[4:5], v6, off
	global_store_dword v[4:5], v7, off offset:2048
	v_add_co_u32_e32 v4, vcc, s9, v36
	s_mov_b32 s9, 0x479e5000
	s_nop 0
	v_addc_co_u32_e32 v5, vcc, 0, v37, vcc
	global_store_dword v[4:5], v8, off
	global_store_dword v[4:5], v9, off offset:2048
	v_add_co_u32_e32 v4, vcc, s9, v36
	s_mov_b32 s9, 0x479e8000
	s_nop 0
	v_addc_co_u32_e32 v5, vcc, 0, v37, vcc
	global_store_dword v[4:5], v10, off
	global_store_dword v[4:5], v11, off offset:2048
	v_add_co_u32_e32 v4, vcc, s9, v36
	s_mov_b32 s9, 0x479e9000
	s_nop 0
	v_addc_co_u32_e32 v5, vcc, 0, v37, vcc
	global_store_dword v[4:5], v12, off
	global_store_dword v[4:5], v13, off offset:2048
	v_add_co_u32_e32 v4, vcc, s9, v36
	s_mov_b32 s9, 0x479ec000
	s_nop 0
	v_addc_co_u32_e32 v5, vcc, 0, v37, vcc
	global_store_dword v[4:5], v14, off
	global_store_dword v[4:5], v15, off offset:2048
	v_add_co_u32_e32 v4, vcc, s9, v36
	s_mov_b32 s9, 0x479ed000
	s_nop 0
	v_addc_co_u32_e32 v5, vcc, 0, v37, vcc
	global_store_dword v[4:5], v16, off
	global_store_dword v[4:5], v17, off offset:2048
	v_add_co_u32_e32 v4, vcc, s9, v36
	s_mov_b32 s9, 0x479f0000
	s_nop 0
	v_addc_co_u32_e32 v5, vcc, 0, v37, vcc
	global_store_dword v[4:5], v18, off
	global_store_dword v[4:5], v19, off offset:2048
	v_add_co_u32_e32 v4, vcc, s9, v36
	s_mov_b32 s9, 0x479f1000
	s_nop 0
	v_addc_co_u32_e32 v5, vcc, 0, v37, vcc
	global_store_dword v[4:5], v20, off
	global_store_dword v[4:5], v21, off offset:2048
	v_add_co_u32_e32 v4, vcc, s9, v36
	s_mov_b32 s9, 0x479f4000
	s_nop 0
	v_addc_co_u32_e32 v5, vcc, 0, v37, vcc
	global_store_dword v[4:5], v22, off
	global_store_dword v[4:5], v23, off offset:2048
	v_add_co_u32_e32 v4, vcc, s9, v36
	s_mov_b32 s9, 0x479f5000
	s_nop 0
	v_addc_co_u32_e32 v5, vcc, 0, v37, vcc
	global_store_dword v[4:5], v24, off
	global_store_dword v[4:5], v25, off offset:2048
	v_add_co_u32_e32 v4, vcc, s9, v36
	s_mov_b32 s9, 0x479f8000
	s_nop 0
	v_addc_co_u32_e32 v5, vcc, 0, v37, vcc
	global_store_dword v[4:5], v26, off
	global_store_dword v[4:5], v27, off offset:2048
	v_add_co_u32_e32 v4, vcc, s9, v36
	s_mov_b32 s9, 0x479f9000
	s_nop 0
	v_addc_co_u32_e32 v5, vcc, 0, v37, vcc
	global_store_dword v[4:5], v28, off
	global_store_dword v[4:5], v29, off offset:2048
	v_add_co_u32_e32 v4, vcc, s9, v36
	s_mov_b32 s9, 0x479fc000
	s_nop 0
	v_addc_co_u32_e32 v5, vcc, 0, v37, vcc
	global_store_dword v[4:5], v30, off
	global_store_dword v[4:5], v31, off offset:2048
	v_add_co_u32_e32 v4, vcc, s9, v36
	s_nop 1
	v_addc_co_u32_e32 v5, vcc, 0, v37, vcc
	global_store_dword v[4:5], v32, off
	global_store_dword v[4:5], v33, off offset:2048
	v_add_co_u32_e32 v4, vcc, 0x479fd000, v36
	s_nop 1
	v_addc_co_u32_e32 v5, vcc, 0, v37, vcc
	global_store_dword v[4:5], v34, off
	global_store_dword v[4:5], v35, off offset:2048
	s_mov_b64 s[28:29], 0
	s_waitcnt lgkmcnt(0)
	s_barrier
